# speedup vs baseline: 1.0081x; 1.0081x over previous
_Z8dog_mainPKfS0_S0_S0_S0_S0_S0_Pf:
	s_load_dwordx8 s[12:19], s[0:1], 0x0
	s_load_dwordx8 s[20:27], s[0:1], 0x20
	s_and_b32 s3, s2, 7
	s_lshl_b32 s3, s3, 5
	s_lshr_b32 s4, s2, 3
	s_add_i32 s4, s3, s4
	s_and_b32 s6, s4, 3
	s_lshr_b32 s7, s4, 2
	s_mov_b32 s5, 0
	s_lshl_b64 s[8:9], s[4:5], 18
	v_and_b32_e32 v1, 63, v0
	v_lshrrev_b32_e32 v2, 6, v0
	v_and_b32_e32 v3, 31, v0
	v_lshl_or_b32 v4, v2, 5, v3
	v_lshlrev_b32_e32 v5, 2, v4
	v_lshlrev_b32_e32 v6, 4, v1
	v_lshl_or_b32 v6, v2, 15, v6
	v_bfe_u32 v7, v0, 5, 1
	s_waitcnt lgkmcnt(0)
	global_load_dword v20, v5, s[18:19]
	global_load_dword v21, v5, s[20:21]
	global_load_dword v22, v5, s[22:23]
	global_load_dword v23, v5, s[24:25]
	global_load_dword v24, v5, s[14:15]
	global_load_dword v25, v5, s[16:17]
	s_add_u32 s12, s12, s8
	s_addc_u32 s13, s13, s9
	v_lshlrev_b32_e32 v6, 4, v1
	v_lshl_or_b32 v6, v2, 12, v6
	global_load_dwordx4 v[128:131], v6, s[12:13] offset:0 nt
	global_load_dwordx4 v[132:135], v6, s[12:13] offset:1024 nt
	global_load_dwordx4 v[136:139], v6, s[12:13] offset:2048 nt
	global_load_dwordx4 v[140:143], v6, s[12:13] offset:3072 nt
	v_add_u32_e32 v6, 0x8000, v6
	global_load_dwordx4 v[144:147], v6, s[12:13] offset:0 nt
	global_load_dwordx4 v[148:151], v6, s[12:13] offset:1024 nt
	global_load_dwordx4 v[152:155], v6, s[12:13] offset:2048 nt
	global_load_dwordx4 v[156:159], v6, s[12:13] offset:3072 nt
	v_add_u32_e32 v6, 0x8000, v6
	global_load_dwordx4 v[160:163], v6, s[12:13] offset:0 nt
	global_load_dwordx4 v[164:167], v6, s[12:13] offset:1024 nt
	global_load_dwordx4 v[168:171], v6, s[12:13] offset:2048 nt
	global_load_dwordx4 v[172:175], v6, s[12:13] offset:3072 nt
	v_add_u32_e32 v6, 0x8000, v6
	global_load_dwordx4 v[176:179], v6, s[12:13] offset:0 nt
	global_load_dwordx4 v[180:183], v6, s[12:13] offset:1024 nt
	global_load_dwordx4 v[184:187], v6, s[12:13] offset:2048 nt
	global_load_dwordx4 v[188:191], v6, s[12:13] offset:3072 nt
	v_add_u32_e32 v6, 0x8000, v6
	global_load_dwordx4 v[192:195], v6, s[12:13] offset:0 nt
	global_load_dwordx4 v[196:199], v6, s[12:13] offset:1024 nt
	global_load_dwordx4 v[200:203], v6, s[12:13] offset:2048 nt
	global_load_dwordx4 v[204:207], v6, s[12:13] offset:3072 nt
	v_add_u32_e32 v6, 0x8000, v6
	global_load_dwordx4 v[208:211], v6, s[12:13] offset:0 nt
	global_load_dwordx4 v[212:215], v6, s[12:13] offset:1024 nt
	global_load_dwordx4 v[216:219], v6, s[12:13] offset:2048 nt
	global_load_dwordx4 v[220:223], v6, s[12:13] offset:3072 nt
	v_add_u32_e32 v6, 0x8000, v6
	global_load_dwordx4 v[224:227], v6, s[12:13] offset:0 nt
	global_load_dwordx4 v[228:231], v6, s[12:13] offset:1024 nt
	global_load_dwordx4 v[232:235], v6, s[12:13] offset:2048 nt
	global_load_dwordx4 v[236:239], v6, s[12:13] offset:3072 nt
	v_add_u32_e32 v6, 0x8000, v6
	global_load_dwordx4 v[240:243], v6, s[12:13] offset:0 nt
	global_load_dwordx4 v[244:247], v6, s[12:13] offset:1024 nt
	global_load_dwordx4 v[248:251], v6, s[12:13] offset:2048 nt
	global_load_dwordx4 v[252:255], v6, s[12:13] offset:3072 nt
	v_and_b32_e32 v16, 1, v0
	v_cmp_eq_u32_e64 s[30:31], 0, v16
	v_and_b32_e32 v17, 2, v0
	v_cmp_eq_u32_e64 s[32:33], 0, v17
	v_and_b32_e32 v16, 3, v0
	v_lshrrev_b32_e32 v17, 2, v1
	v_lshlrev_b32_e32 v16, 5, v16
	v_lshl_add_u32 v16, v17, 1, v16
	v_lshrrev_b32_e32 v17, 1, v2
	s_movk_i32 s10, 0x110
	v_mad_u32_u24 v16, v17, s10, v16
	v_and_b32_e32 v17, 1, v2
	v_lshl_add_u32 v14, v17, 7, v16
	s_movk_i32 s10, 0x110
	v_lshlrev_b32_e32 v17, 4, v7
	v_mad_u32_u24 v15, v3, s10, v17
	s_lshl_b32 s11, s6, 5
	v_lshl_add_u32 v18, v7, 2, s11
	v_cvt_f32_u32_e32 v18, v18
	v_lshlrev_b32_e32 v19, 3, v7
	v_cvt_f32_u32_e32 v19, v19
	s_waitcnt vmcnt(32)
	v_add_f32_e32 v26, v20, v21
	v_rcp_f32_e32 v27, v20
	v_rcp_f32_e32 v28, v26
	v_sub_f32_e32 v12, v19, v22
	v_sub_f32_e32 v13, v18, v23
	v_fma_f32 v29, -v20, v27, 1.0
	v_fma_f32 v30, -v26, v28, 1.0
	v_fma_f32 v27, v29, v27, v27
	v_fma_f32 v28, v30, v28, v28
	v_mul_f32_e32 v8, 0xbf38aa3b, v27
	v_mul_f32_e32 v9, 0xbf38aa3b, v28
	v_mul_f32_e32 v29, v24, v27
	v_mul_f32_e32 v30, v25, v28
	v_mul_f32_e32 v10, 0x3e22f983, v29
	v_mul_f32_e32 v11, 0x3e22f983, v30
	v_mul_f32_e32 v16, v12, v12
	v_add_f32_e32 v17, 0x3f800000, v12
	v_add_f32_e32 v18, 0x40000000, v12
	v_add_f32_e32 v19, 0x40400000, v12
	v_mul_f32_e32 v17, v17, v17
	v_mul_f32_e32 v18, v18, v18
	v_mul_f32_e32 v19, v19, v19
	v_mul_f32_e32 v20, v8, v16
	v_mul_f32_e32 v24, v9, v16
	v_mul_f32_e32 v21, v8, v17
	v_mul_f32_e32 v25, v9, v17
	v_mul_f32_e32 v22, v8, v18
	v_mul_f32_e32 v26, v9, v18
	v_mul_f32_e32 v23, v8, v19
	v_mul_f32_e32 v27, v9, v19
	v_exp_f32_e32 v20, v20
	v_exp_f32_e32 v21, v21
	v_exp_f32_e32 v22, v22
	v_exp_f32_e32 v23, v23
	v_exp_f32_e32 v24, v24
	v_exp_f32_e32 v25, v25
	v_exp_f32_e32 v26, v26
	v_exp_f32_e32 v27, v27
	v_cvt_pk_f16_f32 v32, v20, v21
	v_cvt_pk_f16_f32 v33, v22, v23
	v_cvt_pk_f16_f32 v64, v24, v25
	v_cvt_pk_f16_f32 v65, v26, v27
	v_add_f32_e32 v16, 0x40800000, v12
	v_add_f32_e32 v17, 0x40a00000, v12
	v_add_f32_e32 v18, 0x40c00000, v12
	v_add_f32_e32 v19, 0x40e00000, v12
	v_mul_f32_e32 v16, v16, v16
	v_mul_f32_e32 v17, v17, v17
	v_mul_f32_e32 v18, v18, v18
	v_mul_f32_e32 v19, v19, v19
	v_mul_f32_e32 v20, v8, v16
	v_mul_f32_e32 v24, v9, v16
	v_mul_f32_e32 v21, v8, v17
	v_mul_f32_e32 v25, v9, v17
	v_mul_f32_e32 v22, v8, v18
	v_mul_f32_e32 v26, v9, v18
	v_mul_f32_e32 v23, v8, v19
	v_mul_f32_e32 v27, v9, v19
	v_exp_f32_e32 v20, v20
	v_exp_f32_e32 v21, v21
	v_exp_f32_e32 v22, v22
	v_exp_f32_e32 v23, v23
	v_exp_f32_e32 v24, v24
	v_exp_f32_e32 v25, v25
	v_exp_f32_e32 v26, v26
	v_exp_f32_e32 v27, v27
	v_cvt_pk_f16_f32 v34, v20, v21
	v_cvt_pk_f16_f32 v35, v22, v23
	v_cvt_pk_f16_f32 v66, v24, v25
	v_cvt_pk_f16_f32 v67, v26, v27
	v_add_f32_e32 v16, 0x41800000, v12
	v_add_f32_e32 v17, 0x41880000, v12
	v_add_f32_e32 v18, 0x41900000, v12
	v_add_f32_e32 v19, 0x41980000, v12
	v_mul_f32_e32 v16, v16, v16
	v_mul_f32_e32 v17, v17, v17
	v_mul_f32_e32 v18, v18, v18
	v_mul_f32_e32 v19, v19, v19
	v_mul_f32_e32 v20, v8, v16
	v_mul_f32_e32 v24, v9, v16
	v_mul_f32_e32 v21, v8, v17
	v_mul_f32_e32 v25, v9, v17
	v_mul_f32_e32 v22, v8, v18
	v_mul_f32_e32 v26, v9, v18
	v_mul_f32_e32 v23, v8, v19
	v_mul_f32_e32 v27, v9, v19
	v_exp_f32_e32 v20, v20
	v_exp_f32_e32 v21, v21
	v_exp_f32_e32 v22, v22
	v_exp_f32_e32 v23, v23
	v_exp_f32_e32 v24, v24
	v_exp_f32_e32 v25, v25
	v_exp_f32_e32 v26, v26
	v_exp_f32_e32 v27, v27
	v_cvt_pk_f16_f32 v36, v20, v21
	v_cvt_pk_f16_f32 v37, v22, v23
	v_cvt_pk_f16_f32 v68, v24, v25
	v_cvt_pk_f16_f32 v69, v26, v27
	v_add_f32_e32 v16, 0x41a00000, v12
	v_add_f32_e32 v17, 0x41a80000, v12
	v_add_f32_e32 v18, 0x41b00000, v12
	v_add_f32_e32 v19, 0x41b80000, v12
	v_mul_f32_e32 v16, v16, v16
	v_mul_f32_e32 v17, v17, v17
	v_mul_f32_e32 v18, v18, v18
	v_mul_f32_e32 v19, v19, v19
	v_mul_f32_e32 v20, v8, v16
	v_mul_f32_e32 v24, v9, v16
	v_mul_f32_e32 v21, v8, v17
	v_mul_f32_e32 v25, v9, v17
	v_mul_f32_e32 v22, v8, v18
	v_mul_f32_e32 v26, v9, v18
	v_mul_f32_e32 v23, v8, v19
	v_mul_f32_e32 v27, v9, v19
	v_exp_f32_e32 v20, v20
	v_exp_f32_e32 v21, v21
	v_exp_f32_e32 v22, v22
	v_exp_f32_e32 v23, v23
	v_exp_f32_e32 v24, v24
	v_exp_f32_e32 v25, v25
	v_exp_f32_e32 v26, v26
	v_exp_f32_e32 v27, v27
	v_cvt_pk_f16_f32 v38, v20, v21
	v_cvt_pk_f16_f32 v39, v22, v23
	v_cvt_pk_f16_f32 v70, v24, v25
	v_cvt_pk_f16_f32 v71, v26, v27
	v_add_f32_e32 v16, 0x42000000, v12
	v_add_f32_e32 v17, 0x42040000, v12
	v_add_f32_e32 v18, 0x42080000, v12
	v_add_f32_e32 v19, 0x420c0000, v12
	v_mul_f32_e32 v16, v16, v16
	v_mul_f32_e32 v17, v17, v17
	v_mul_f32_e32 v18, v18, v18
	v_mul_f32_e32 v19, v19, v19
	v_mul_f32_e32 v20, v8, v16
	v_mul_f32_e32 v24, v9, v16
	v_mul_f32_e32 v21, v8, v17
	v_mul_f32_e32 v25, v9, v17
	v_mul_f32_e32 v22, v8, v18
	v_mul_f32_e32 v26, v9, v18
	v_mul_f32_e32 v23, v8, v19
	v_mul_f32_e32 v27, v9, v19
	v_exp_f32_e32 v20, v20
	v_exp_f32_e32 v21, v21
	v_exp_f32_e32 v22, v22
	v_exp_f32_e32 v23, v23
	v_exp_f32_e32 v24, v24
	v_exp_f32_e32 v25, v25
	v_exp_f32_e32 v26, v26
	v_exp_f32_e32 v27, v27
	v_cvt_pk_f16_f32 v40, v20, v21
	v_cvt_pk_f16_f32 v41, v22, v23
	v_cvt_pk_f16_f32 v72, v24, v25
	v_cvt_pk_f16_f32 v73, v26, v27
	v_add_f32_e32 v16, 0x42100000, v12
	v_add_f32_e32 v17, 0x42140000, v12
	v_add_f32_e32 v18, 0x42180000, v12
	v_add_f32_e32 v19, 0x421c0000, v12
	v_mul_f32_e32 v16, v16, v16
	v_mul_f32_e32 v17, v17, v17
	v_mul_f32_e32 v18, v18, v18
	v_mul_f32_e32 v19, v19, v19
	v_mul_f32_e32 v20, v8, v16
	v_mul_f32_e32 v24, v9, v16
	v_mul_f32_e32 v21, v8, v17
	v_mul_f32_e32 v25, v9, v17
	v_mul_f32_e32 v22, v8, v18
	v_mul_f32_e32 v26, v9, v18
	v_mul_f32_e32 v23, v8, v19
	v_mul_f32_e32 v27, v9, v19
	v_exp_f32_e32 v20, v20
	v_exp_f32_e32 v21, v21
	v_exp_f32_e32 v22, v22
	v_exp_f32_e32 v23, v23
	v_exp_f32_e32 v24, v24
	v_exp_f32_e32 v25, v25
	v_exp_f32_e32 v26, v26
	v_exp_f32_e32 v27, v27
	v_cvt_pk_f16_f32 v42, v20, v21
	v_cvt_pk_f16_f32 v43, v22, v23
	v_cvt_pk_f16_f32 v74, v24, v25
	v_cvt_pk_f16_f32 v75, v26, v27
	v_add_f32_e32 v16, 0x42400000, v12
	v_add_f32_e32 v17, 0x42440000, v12
	v_add_f32_e32 v18, 0x42480000, v12
	v_add_f32_e32 v19, 0x424c0000, v12
	v_mul_f32_e32 v16, v16, v16
	v_mul_f32_e32 v17, v17, v17
	v_mul_f32_e32 v18, v18, v18
	v_mul_f32_e32 v19, v19, v19
	v_mul_f32_e32 v20, v8, v16
	v_mul_f32_e32 v24, v9, v16
	v_mul_f32_e32 v21, v8, v17
	v_mul_f32_e32 v25, v9, v17
	v_mul_f32_e32 v22, v8, v18
	v_mul_f32_e32 v26, v9, v18
	v_mul_f32_e32 v23, v8, v19
	v_mul_f32_e32 v27, v9, v19
	v_exp_f32_e32 v20, v20
	v_exp_f32_e32 v21, v21
	v_exp_f32_e32 v22, v22
	v_exp_f32_e32 v23, v23
	v_exp_f32_e32 v24, v24
	v_exp_f32_e32 v25, v25
	v_exp_f32_e32 v26, v26
	v_exp_f32_e32 v27, v27
	v_cvt_pk_f16_f32 v44, v20, v21
	v_cvt_pk_f16_f32 v45, v22, v23
	v_cvt_pk_f16_f32 v76, v24, v25
	v_cvt_pk_f16_f32 v77, v26, v27
	v_add_f32_e32 v16, 0x42500000, v12
	v_add_f32_e32 v17, 0x42540000, v12
	v_add_f32_e32 v18, 0x42580000, v12
	v_add_f32_e32 v19, 0x425c0000, v12
	v_mul_f32_e32 v16, v16, v16
	v_mul_f32_e32 v17, v17, v17
	v_mul_f32_e32 v18, v18, v18
	v_mul_f32_e32 v19, v19, v19
	v_mul_f32_e32 v20, v8, v16
	v_mul_f32_e32 v24, v9, v16
	v_mul_f32_e32 v21, v8, v17
	v_mul_f32_e32 v25, v9, v17
	v_mul_f32_e32 v22, v8, v18
	v_mul_f32_e32 v26, v9, v18
	v_mul_f32_e32 v23, v8, v19
	v_mul_f32_e32 v27, v9, v19
	v_exp_f32_e32 v20, v20
	v_exp_f32_e32 v21, v21
	v_exp_f32_e32 v22, v22
	v_exp_f32_e32 v23, v23
	v_exp_f32_e32 v24, v24
	v_exp_f32_e32 v25, v25
	v_exp_f32_e32 v26, v26
	v_exp_f32_e32 v27, v27
	v_cvt_pk_f16_f32 v46, v20, v21
	v_cvt_pk_f16_f32 v47, v22, v23
	v_cvt_pk_f16_f32 v78, v24, v25
	v_cvt_pk_f16_f32 v79, v26, v27
	v_add_f32_e32 v16, 0x42800000, v12
	v_add_f32_e32 v17, 0x42820000, v12
	v_add_f32_e32 v18, 0x42840000, v12
	v_add_f32_e32 v19, 0x42860000, v12
	v_mul_f32_e32 v16, v16, v16
	v_mul_f32_e32 v17, v17, v17
	v_mul_f32_e32 v18, v18, v18
	v_mul_f32_e32 v19, v19, v19
	v_mul_f32_e32 v20, v8, v16
	v_mul_f32_e32 v24, v9, v16
	v_mul_f32_e32 v21, v8, v17
	v_mul_f32_e32 v25, v9, v17
	v_mul_f32_e32 v22, v8, v18
	v_mul_f32_e32 v26, v9, v18
	v_mul_f32_e32 v23, v8, v19
	v_mul_f32_e32 v27, v9, v19
	v_exp_f32_e32 v20, v20
	v_exp_f32_e32 v21, v21
	v_exp_f32_e32 v22, v22
	v_exp_f32_e32 v23, v23
	v_exp_f32_e32 v24, v24
	v_exp_f32_e32 v25, v25
	v_exp_f32_e32 v26, v26
	v_exp_f32_e32 v27, v27
	v_cvt_pk_f16_f32 v48, v20, v21
	v_cvt_pk_f16_f32 v49, v22, v23
	v_cvt_pk_f16_f32 v80, v24, v25
	v_cvt_pk_f16_f32 v81, v26, v27
	v_add_f32_e32 v16, 0x42880000, v12
	v_add_f32_e32 v17, 0x428a0000, v12
	v_add_f32_e32 v18, 0x428c0000, v12
	v_add_f32_e32 v19, 0x428e0000, v12
	v_mul_f32_e32 v16, v16, v16
	v_mul_f32_e32 v17, v17, v17
	v_mul_f32_e32 v18, v18, v18
	v_mul_f32_e32 v19, v19, v19
	v_mul_f32_e32 v20, v8, v16
	v_mul_f32_e32 v24, v9, v16
	v_mul_f32_e32 v21, v8, v17
	v_mul_f32_e32 v25, v9, v17
	v_mul_f32_e32 v22, v8, v18
	v_mul_f32_e32 v26, v9, v18
	v_mul_f32_e32 v23, v8, v19
	v_mul_f32_e32 v27, v9, v19
	v_exp_f32_e32 v20, v20
	v_exp_f32_e32 v21, v21
	v_exp_f32_e32 v22, v22
	v_exp_f32_e32 v23, v23
	v_exp_f32_e32 v24, v24
	v_exp_f32_e32 v25, v25
	v_exp_f32_e32 v26, v26
	v_exp_f32_e32 v27, v27
	v_cvt_pk_f16_f32 v50, v20, v21
	v_cvt_pk_f16_f32 v51, v22, v23
	v_cvt_pk_f16_f32 v82, v24, v25
	v_cvt_pk_f16_f32 v83, v26, v27
	v_add_f32_e32 v16, 0x42a00000, v12
	v_add_f32_e32 v17, 0x42a20000, v12
	v_add_f32_e32 v18, 0x42a40000, v12
	v_add_f32_e32 v19, 0x42a60000, v12
	v_mul_f32_e32 v16, v16, v16
	v_mul_f32_e32 v17, v17, v17
	v_mul_f32_e32 v18, v18, v18
	v_mul_f32_e32 v19, v19, v19
	v_mul_f32_e32 v20, v8, v16
	v_mul_f32_e32 v24, v9, v16
	v_mul_f32_e32 v21, v8, v17
	v_mul_f32_e32 v25, v9, v17
	v_mul_f32_e32 v22, v8, v18
	v_mul_f32_e32 v26, v9, v18
	v_mul_f32_e32 v23, v8, v19
	v_mul_f32_e32 v27, v9, v19
	v_exp_f32_e32 v20, v20
	v_exp_f32_e32 v21, v21
	v_exp_f32_e32 v22, v22
	v_exp_f32_e32 v23, v23
	v_exp_f32_e32 v24, v24
	v_exp_f32_e32 v25, v25
	v_exp_f32_e32 v26, v26
	v_exp_f32_e32 v27, v27
	v_cvt_pk_f16_f32 v52, v20, v21
	v_cvt_pk_f16_f32 v53, v22, v23
	v_cvt_pk_f16_f32 v84, v24, v25
	v_cvt_pk_f16_f32 v85, v26, v27
	v_add_f32_e32 v16, 0x42a80000, v12
	v_add_f32_e32 v17, 0x42aa0000, v12
	v_add_f32_e32 v18, 0x42ac0000, v12
	v_add_f32_e32 v19, 0x42ae0000, v12
	v_mul_f32_e32 v16, v16, v16
	v_mul_f32_e32 v17, v17, v17
	v_mul_f32_e32 v18, v18, v18
	v_mul_f32_e32 v19, v19, v19
	v_mul_f32_e32 v20, v8, v16
	v_mul_f32_e32 v24, v9, v16
	v_mul_f32_e32 v21, v8, v17
	v_mul_f32_e32 v25, v9, v17
	v_mul_f32_e32 v22, v8, v18
	v_mul_f32_e32 v26, v9, v18
	v_mul_f32_e32 v23, v8, v19
	v_mul_f32_e32 v27, v9, v19
	v_exp_f32_e32 v20, v20
	v_exp_f32_e32 v21, v21
	v_exp_f32_e32 v22, v22
	v_exp_f32_e32 v23, v23
	v_exp_f32_e32 v24, v24
	v_exp_f32_e32 v25, v25
	v_exp_f32_e32 v26, v26
	v_exp_f32_e32 v27, v27
	v_cvt_pk_f16_f32 v54, v20, v21
	v_cvt_pk_f16_f32 v55, v22, v23
	v_cvt_pk_f16_f32 v86, v24, v25
	v_cvt_pk_f16_f32 v87, v26, v27
	v_add_f32_e32 v16, 0x42c00000, v12
	v_add_f32_e32 v17, 0x42c20000, v12
	v_add_f32_e32 v18, 0x42c40000, v12
	v_add_f32_e32 v19, 0x42c60000, v12
	v_mul_f32_e32 v16, v16, v16
	v_mul_f32_e32 v17, v17, v17
	v_mul_f32_e32 v18, v18, v18
	v_mul_f32_e32 v19, v19, v19
	v_mul_f32_e32 v20, v8, v16
	v_mul_f32_e32 v24, v9, v16
	v_mul_f32_e32 v21, v8, v17
	v_mul_f32_e32 v25, v9, v17
	v_mul_f32_e32 v22, v8, v18
	v_mul_f32_e32 v26, v9, v18
	v_mul_f32_e32 v23, v8, v19
	v_mul_f32_e32 v27, v9, v19
	v_exp_f32_e32 v20, v20
	v_exp_f32_e32 v21, v21
	v_exp_f32_e32 v22, v22
	v_exp_f32_e32 v23, v23
	v_exp_f32_e32 v24, v24
	v_exp_f32_e32 v25, v25
	v_exp_f32_e32 v26, v26
	v_exp_f32_e32 v27, v27
	v_cvt_pk_f16_f32 v56, v20, v21
	v_cvt_pk_f16_f32 v57, v22, v23
	v_cvt_pk_f16_f32 v88, v24, v25
	v_cvt_pk_f16_f32 v89, v26, v27
	v_add_f32_e32 v16, 0x42c80000, v12
	v_add_f32_e32 v17, 0x42ca0000, v12
	v_add_f32_e32 v18, 0x42cc0000, v12
	v_add_f32_e32 v19, 0x42ce0000, v12
	v_mul_f32_e32 v16, v16, v16
	v_mul_f32_e32 v17, v17, v17
	v_mul_f32_e32 v18, v18, v18
	v_mul_f32_e32 v19, v19, v19
	v_mul_f32_e32 v20, v8, v16
	v_mul_f32_e32 v24, v9, v16
	v_mul_f32_e32 v21, v8, v17
	v_mul_f32_e32 v25, v9, v17
	v_mul_f32_e32 v22, v8, v18
	v_mul_f32_e32 v26, v9, v18
	v_mul_f32_e32 v23, v8, v19
	v_mul_f32_e32 v27, v9, v19
	v_exp_f32_e32 v20, v20
	v_exp_f32_e32 v21, v21
	v_exp_f32_e32 v22, v22
	v_exp_f32_e32 v23, v23
	v_exp_f32_e32 v24, v24
	v_exp_f32_e32 v25, v25
	v_exp_f32_e32 v26, v26
	v_exp_f32_e32 v27, v27
	v_cvt_pk_f16_f32 v58, v20, v21
	v_cvt_pk_f16_f32 v59, v22, v23
	v_cvt_pk_f16_f32 v90, v24, v25
	v_cvt_pk_f16_f32 v91, v26, v27
	v_add_f32_e32 v16, 0x42e00000, v12
	v_add_f32_e32 v17, 0x42e20000, v12
	v_add_f32_e32 v18, 0x42e40000, v12
	v_add_f32_e32 v19, 0x42e60000, v12
	v_mul_f32_e32 v16, v16, v16
	v_mul_f32_e32 v17, v17, v17
	v_mul_f32_e32 v18, v18, v18
	v_mul_f32_e32 v19, v19, v19
	v_mul_f32_e32 v20, v8, v16
	v_mul_f32_e32 v24, v9, v16
	v_mul_f32_e32 v21, v8, v17
	v_mul_f32_e32 v25, v9, v17
	v_mul_f32_e32 v22, v8, v18
	v_mul_f32_e32 v26, v9, v18
	v_mul_f32_e32 v23, v8, v19
	v_mul_f32_e32 v27, v9, v19
	v_exp_f32_e32 v20, v20
	v_exp_f32_e32 v21, v21
	v_exp_f32_e32 v22, v22
	v_exp_f32_e32 v23, v23
	v_exp_f32_e32 v24, v24
	v_exp_f32_e32 v25, v25
	v_exp_f32_e32 v26, v26
	v_exp_f32_e32 v27, v27
	v_cvt_pk_f16_f32 v60, v20, v21
	v_cvt_pk_f16_f32 v61, v22, v23
	v_cvt_pk_f16_f32 v92, v24, v25
	v_cvt_pk_f16_f32 v93, v26, v27
	v_add_f32_e32 v16, 0x42e80000, v12
	v_add_f32_e32 v17, 0x42ea0000, v12
	v_add_f32_e32 v18, 0x42ec0000, v12
	v_add_f32_e32 v19, 0x42ee0000, v12
	v_mul_f32_e32 v16, v16, v16
	v_mul_f32_e32 v17, v17, v17
	v_mul_f32_e32 v18, v18, v18
	v_mul_f32_e32 v19, v19, v19
	v_mul_f32_e32 v20, v8, v16
	v_mul_f32_e32 v24, v9, v16
	v_mul_f32_e32 v21, v8, v17
	v_mul_f32_e32 v25, v9, v17
	v_mul_f32_e32 v22, v8, v18
	v_mul_f32_e32 v26, v9, v18
	v_mul_f32_e32 v23, v8, v19
	v_mul_f32_e32 v27, v9, v19
	v_exp_f32_e32 v20, v20
	v_exp_f32_e32 v21, v21
	v_exp_f32_e32 v22, v22
	v_exp_f32_e32 v23, v23
	v_exp_f32_e32 v24, v24
	v_exp_f32_e32 v25, v25
	v_exp_f32_e32 v26, v26
	v_exp_f32_e32 v27, v27
	v_cvt_pk_f16_f32 v62, v20, v21
	v_cvt_pk_f16_f32 v63, v22, v23
	v_cvt_pk_f16_f32 v94, v24, v25
	v_cvt_pk_f16_f32 v95, v26, v27
	v_mul_f32_e32 v16, v13, v13
	v_add_f32_e32 v17, 0x3f800000, v13
	v_add_f32_e32 v18, 0x40000000, v13
	v_add_f32_e32 v19, 0x40400000, v13
	v_mul_f32_e32 v17, v17, v17
	v_mul_f32_e32 v18, v18, v18
	v_mul_f32_e32 v19, v19, v19
	v_mul_f32_e32 v20, v8, v16
	v_mul_f32_e32 v24, v9, v16
	v_mul_f32_e32 v21, v8, v17
	v_mul_f32_e32 v25, v9, v17
	v_mul_f32_e32 v22, v8, v18
	v_mul_f32_e32 v26, v9, v18
	v_mul_f32_e32 v23, v8, v19
	v_mul_f32_e32 v27, v9, v19
	v_exp_f32_e32 v20, v20
	v_exp_f32_e32 v21, v21
	v_exp_f32_e32 v22, v22
	v_exp_f32_e32 v23, v23
	v_exp_f32_e32 v24, v24
	v_exp_f32_e32 v25, v25
	v_exp_f32_e32 v26, v26
	v_exp_f32_e32 v27, v27
	v_mul_f32_e32 v96, v10, v20
	v_mul_f32_e32 v97, v10, v21
	v_mul_f32_e32 v98, v10, v22
	v_mul_f32_e32 v99, v10, v23
	v_mul_f32_e32 v112, v11, v24
	v_mul_f32_e32 v113, v11, v25
	v_mul_f32_e32 v114, v11, v26
	v_mul_f32_e32 v115, v11, v27
	v_add_f32_e32 v16, 0x41000000, v13
	v_add_f32_e32 v17, 0x41100000, v13
	v_add_f32_e32 v18, 0x41200000, v13
	v_add_f32_e32 v19, 0x41300000, v13
	v_mul_f32_e32 v16, v16, v16
	v_mul_f32_e32 v17, v17, v17
	v_mul_f32_e32 v18, v18, v18
	v_mul_f32_e32 v19, v19, v19
	v_mul_f32_e32 v20, v8, v16
	v_mul_f32_e32 v24, v9, v16
	v_mul_f32_e32 v21, v8, v17
	v_mul_f32_e32 v25, v9, v17
	v_mul_f32_e32 v22, v8, v18
	v_mul_f32_e32 v26, v9, v18
	v_mul_f32_e32 v23, v8, v19
	v_mul_f32_e32 v27, v9, v19
	v_exp_f32_e32 v20, v20
	v_exp_f32_e32 v21, v21
	v_exp_f32_e32 v22, v22
	v_exp_f32_e32 v23, v23
	v_exp_f32_e32 v24, v24
	v_exp_f32_e32 v25, v25
	v_exp_f32_e32 v26, v26
	v_exp_f32_e32 v27, v27
	v_mul_f32_e32 v100, v10, v20
	v_mul_f32_e32 v101, v10, v21
	v_mul_f32_e32 v102, v10, v22
	v_mul_f32_e32 v103, v10, v23
	v_mul_f32_e32 v116, v11, v24
	v_mul_f32_e32 v117, v11, v25
	v_mul_f32_e32 v118, v11, v26
	v_mul_f32_e32 v119, v11, v27
	v_add_f32_e32 v16, 0x41800000, v13
	v_add_f32_e32 v17, 0x41880000, v13
	v_add_f32_e32 v18, 0x41900000, v13
	v_add_f32_e32 v19, 0x41980000, v13
	v_mul_f32_e32 v16, v16, v16
	v_mul_f32_e32 v17, v17, v17
	v_mul_f32_e32 v18, v18, v18
	v_mul_f32_e32 v19, v19, v19
	v_mul_f32_e32 v20, v8, v16
	v_mul_f32_e32 v24, v9, v16
	v_mul_f32_e32 v21, v8, v17
	v_mul_f32_e32 v25, v9, v17
	v_mul_f32_e32 v22, v8, v18
	v_mul_f32_e32 v26, v9, v18
	v_mul_f32_e32 v23, v8, v19
	v_mul_f32_e32 v27, v9, v19
	v_exp_f32_e32 v20, v20
	v_exp_f32_e32 v21, v21
	v_exp_f32_e32 v22, v22
	v_exp_f32_e32 v23, v23
	v_exp_f32_e32 v24, v24
	v_exp_f32_e32 v25, v25
	v_exp_f32_e32 v26, v26
	v_exp_f32_e32 v27, v27
	v_mul_f32_e32 v104, v10, v20
	v_mul_f32_e32 v105, v10, v21
	v_mul_f32_e32 v106, v10, v22
	v_mul_f32_e32 v107, v10, v23
	v_mul_f32_e32 v120, v11, v24
	v_mul_f32_e32 v121, v11, v25
	v_mul_f32_e32 v122, v11, v26
	v_mul_f32_e32 v123, v11, v27
	v_add_f32_e32 v16, 0x41c00000, v13
	v_add_f32_e32 v17, 0x41c80000, v13
	v_add_f32_e32 v18, 0x41d00000, v13
	v_add_f32_e32 v19, 0x41d80000, v13
	v_mul_f32_e32 v16, v16, v16
	v_mul_f32_e32 v17, v17, v17
	v_mul_f32_e32 v18, v18, v18
	v_mul_f32_e32 v19, v19, v19
	v_mul_f32_e32 v20, v8, v16
	v_mul_f32_e32 v24, v9, v16
	v_mul_f32_e32 v21, v8, v17
	v_mul_f32_e32 v25, v9, v17
	v_mul_f32_e32 v22, v8, v18
	v_mul_f32_e32 v26, v9, v18
	v_mul_f32_e32 v23, v8, v19
	v_mul_f32_e32 v27, v9, v19
	v_exp_f32_e32 v20, v20
	v_exp_f32_e32 v21, v21
	v_exp_f32_e32 v22, v22
	v_exp_f32_e32 v23, v23
	v_exp_f32_e32 v24, v24
	v_exp_f32_e32 v25, v25
	v_exp_f32_e32 v26, v26
	v_exp_f32_e32 v27, v27
	v_mul_f32_e32 v108, v10, v20
	v_mul_f32_e32 v109, v10, v21
	v_mul_f32_e32 v110, v10, v22
	v_mul_f32_e32 v111, v10, v23
	v_mul_f32_e32 v124, v11, v24
	v_mul_f32_e32 v125, v11, v25
	v_mul_f32_e32 v126, v11, v26
	v_mul_f32_e32 v127, v11, v27
	s_waitcnt vmcnt(28)
	v_add_f32_e32 v128, v128, v129
	v_add_f32_e32 v130, v130, v131
	v_add_f32_e32 v132, v132, v133
	v_add_f32_e32 v134, v134, v135
	v_add_f32_e32 v136, v136, v137
	v_add_f32_e32 v138, v138, v139
	v_add_f32_e32 v140, v140, v141
	v_add_f32_e32 v142, v142, v143
	v_add_f32_e32 v128, v128, v130
	v_add_f32_e32 v132, v132, v134
	v_add_f32_e32 v136, v136, v138
	v_add_f32_e32 v140, v140, v142
	v_cndmask_b32_e64 v130, v128, v132, s[30:31]
	v_cndmask_b32_e64 v134, v136, v140, s[30:31]
	v_cndmask_b32_e64 v129, v132, v128, s[30:31]
	v_cndmask_b32_e64 v133, v140, v136, s[30:31]
	v_add_f32_dpp v129, v130, v129 quad_perm:[1,0,3,2] row_mask:0xf bank_mask:0xf bound_ctrl:1
	v_add_f32_dpp v133, v134, v133 quad_perm:[1,0,3,2] row_mask:0xf bank_mask:0xf bound_ctrl:1
	v_cndmask_b32_e64 v135, v129, v133, s[32:33]
	v_cndmask_b32_e64 v131, v133, v129, s[32:33]
	s_nop 1
	v_add_f32_dpp v131, v135, v131 quad_perm:[2,3,0,1] row_mask:0xf bank_mask:0xf bound_ctrl:1
	v_cvt_f16_f32_e32 v131, v131
	ds_write_b16 v14, v131 offset:0
	s_waitcnt vmcnt(24)
	v_add_f32_e32 v144, v144, v145
	v_add_f32_e32 v146, v146, v147
	v_add_f32_e32 v148, v148, v149
	v_add_f32_e32 v150, v150, v151
	v_add_f32_e32 v152, v152, v153
	v_add_f32_e32 v154, v154, v155
	v_add_f32_e32 v156, v156, v157
	v_add_f32_e32 v158, v158, v159
	v_add_f32_e32 v144, v144, v146
	v_add_f32_e32 v148, v148, v150
	v_add_f32_e32 v152, v152, v154
	v_add_f32_e32 v156, v156, v158
	v_cndmask_b32_e64 v146, v144, v148, s[30:31]
	v_cndmask_b32_e64 v150, v152, v156, s[30:31]
	v_cndmask_b32_e64 v145, v148, v144, s[30:31]
	v_cndmask_b32_e64 v149, v156, v152, s[30:31]
	v_add_f32_dpp v145, v146, v145 quad_perm:[1,0,3,2] row_mask:0xf bank_mask:0xf bound_ctrl:1
	v_add_f32_dpp v149, v150, v149 quad_perm:[1,0,3,2] row_mask:0xf bank_mask:0xf bound_ctrl:1
	v_cndmask_b32_e64 v151, v145, v149, s[32:33]
	v_cndmask_b32_e64 v147, v149, v145, s[32:33]
	s_nop 1
	v_add_f32_dpp v147, v151, v147 quad_perm:[2,3,0,1] row_mask:0xf bank_mask:0xf bound_ctrl:1
	v_cvt_f16_f32_e32 v147, v147
	ds_write_b16 v14, v147 offset:1088
	s_waitcnt vmcnt(20)
	v_add_f32_e32 v160, v160, v161
	v_add_f32_e32 v162, v162, v163
	v_add_f32_e32 v164, v164, v165
	v_add_f32_e32 v166, v166, v167
	v_add_f32_e32 v168, v168, v169
	v_add_f32_e32 v170, v170, v171
	v_add_f32_e32 v172, v172, v173
	v_add_f32_e32 v174, v174, v175
	v_add_f32_e32 v160, v160, v162
	v_add_f32_e32 v164, v164, v166
	v_add_f32_e32 v168, v168, v170
	v_add_f32_e32 v172, v172, v174
	v_cndmask_b32_e64 v162, v160, v164, s[30:31]
	v_cndmask_b32_e64 v166, v168, v172, s[30:31]
	v_cndmask_b32_e64 v161, v164, v160, s[30:31]
	v_cndmask_b32_e64 v165, v172, v168, s[30:31]
	v_add_f32_dpp v161, v162, v161 quad_perm:[1,0,3,2] row_mask:0xf bank_mask:0xf bound_ctrl:1
	v_add_f32_dpp v165, v166, v165 quad_perm:[1,0,3,2] row_mask:0xf bank_mask:0xf bound_ctrl:1
	v_cndmask_b32_e64 v167, v161, v165, s[32:33]
	v_cndmask_b32_e64 v163, v165, v161, s[32:33]
	s_nop 1
	v_add_f32_dpp v163, v167, v163 quad_perm:[2,3,0,1] row_mask:0xf bank_mask:0xf bound_ctrl:1
	v_cvt_f16_f32_e32 v163, v163
	ds_write_b16 v14, v163 offset:2176
	s_waitcnt vmcnt(16)
	v_add_f32_e32 v176, v176, v177
	v_add_f32_e32 v178, v178, v179
	v_add_f32_e32 v180, v180, v181
	v_add_f32_e32 v182, v182, v183
	v_add_f32_e32 v184, v184, v185
	v_add_f32_e32 v186, v186, v187
	v_add_f32_e32 v188, v188, v189
	v_add_f32_e32 v190, v190, v191
	v_add_f32_e32 v176, v176, v178
	v_add_f32_e32 v180, v180, v182
	v_add_f32_e32 v184, v184, v186
	v_add_f32_e32 v188, v188, v190
	v_cndmask_b32_e64 v178, v176, v180, s[30:31]
	v_cndmask_b32_e64 v182, v184, v188, s[30:31]
	v_cndmask_b32_e64 v177, v180, v176, s[30:31]
	v_cndmask_b32_e64 v181, v188, v184, s[30:31]
	v_add_f32_dpp v177, v178, v177 quad_perm:[1,0,3,2] row_mask:0xf bank_mask:0xf bound_ctrl:1
	v_add_f32_dpp v181, v182, v181 quad_perm:[1,0,3,2] row_mask:0xf bank_mask:0xf bound_ctrl:1
	v_cndmask_b32_e64 v183, v177, v181, s[32:33]
	v_cndmask_b32_e64 v179, v181, v177, s[32:33]
	s_nop 1
	v_add_f32_dpp v179, v183, v179 quad_perm:[2,3,0,1] row_mask:0xf bank_mask:0xf bound_ctrl:1
	v_cvt_f16_f32_e32 v179, v179
	ds_write_b16 v14, v179 offset:3264
	s_waitcnt vmcnt(12)
	v_add_f32_e32 v192, v192, v193
	v_add_f32_e32 v194, v194, v195
	v_add_f32_e32 v196, v196, v197
	v_add_f32_e32 v198, v198, v199
	v_add_f32_e32 v200, v200, v201
	v_add_f32_e32 v202, v202, v203
	v_add_f32_e32 v204, v204, v205
	v_add_f32_e32 v206, v206, v207
	v_add_f32_e32 v192, v192, v194
	v_add_f32_e32 v196, v196, v198
	v_add_f32_e32 v200, v200, v202
	v_add_f32_e32 v204, v204, v206
	v_cndmask_b32_e64 v194, v192, v196, s[30:31]
	v_cndmask_b32_e64 v198, v200, v204, s[30:31]
	v_cndmask_b32_e64 v193, v196, v192, s[30:31]
	v_cndmask_b32_e64 v197, v204, v200, s[30:31]
	v_add_f32_dpp v193, v194, v193 quad_perm:[1,0,3,2] row_mask:0xf bank_mask:0xf bound_ctrl:1
	v_add_f32_dpp v197, v198, v197 quad_perm:[1,0,3,2] row_mask:0xf bank_mask:0xf bound_ctrl:1
	v_cndmask_b32_e64 v199, v193, v197, s[32:33]
	v_cndmask_b32_e64 v195, v197, v193, s[32:33]
	s_nop 1
	v_add_f32_dpp v195, v199, v195 quad_perm:[2,3,0,1] row_mask:0xf bank_mask:0xf bound_ctrl:1
	v_cvt_f16_f32_e32 v195, v195
	ds_write_b16 v14, v195 offset:4352
	s_waitcnt vmcnt(8)
	v_add_f32_e32 v208, v208, v209
	v_add_f32_e32 v210, v210, v211
	v_add_f32_e32 v212, v212, v213
	v_add_f32_e32 v214, v214, v215
	v_add_f32_e32 v216, v216, v217
	v_add_f32_e32 v218, v218, v219
	v_add_f32_e32 v220, v220, v221
	v_add_f32_e32 v222, v222, v223
	v_add_f32_e32 v208, v208, v210
	v_add_f32_e32 v212, v212, v214
	v_add_f32_e32 v216, v216, v218
	v_add_f32_e32 v220, v220, v222
	v_cndmask_b32_e64 v210, v208, v212, s[30:31]
	v_cndmask_b32_e64 v214, v216, v220, s[30:31]
	v_cndmask_b32_e64 v209, v212, v208, s[30:31]
	v_cndmask_b32_e64 v213, v220, v216, s[30:31]
	v_add_f32_dpp v209, v210, v209 quad_perm:[1,0,3,2] row_mask:0xf bank_mask:0xf bound_ctrl:1
	v_add_f32_dpp v213, v214, v213 quad_perm:[1,0,3,2] row_mask:0xf bank_mask:0xf bound_ctrl:1
	v_cndmask_b32_e64 v215, v209, v213, s[32:33]
	v_cndmask_b32_e64 v211, v213, v209, s[32:33]
	s_nop 1
	v_add_f32_dpp v211, v215, v211 quad_perm:[2,3,0,1] row_mask:0xf bank_mask:0xf bound_ctrl:1
	v_cvt_f16_f32_e32 v211, v211
	ds_write_b16 v14, v211 offset:5440
	s_waitcnt vmcnt(4)
	v_add_f32_e32 v224, v224, v225
	v_add_f32_e32 v226, v226, v227
	v_add_f32_e32 v228, v228, v229
	v_add_f32_e32 v230, v230, v231
	v_add_f32_e32 v232, v232, v233
	v_add_f32_e32 v234, v234, v235
	v_add_f32_e32 v236, v236, v237
	v_add_f32_e32 v238, v238, v239
	v_add_f32_e32 v224, v224, v226
	v_add_f32_e32 v228, v228, v230
	v_add_f32_e32 v232, v232, v234
	v_add_f32_e32 v236, v236, v238
	v_cndmask_b32_e64 v226, v224, v228, s[30:31]
	v_cndmask_b32_e64 v230, v232, v236, s[30:31]
	v_cndmask_b32_e64 v225, v228, v224, s[30:31]
	v_cndmask_b32_e64 v229, v236, v232, s[30:31]
	v_add_f32_dpp v225, v226, v225 quad_perm:[1,0,3,2] row_mask:0xf bank_mask:0xf bound_ctrl:1
	v_add_f32_dpp v229, v230, v229 quad_perm:[1,0,3,2] row_mask:0xf bank_mask:0xf bound_ctrl:1
	v_cndmask_b32_e64 v231, v225, v229, s[32:33]
	v_cndmask_b32_e64 v227, v229, v225, s[32:33]
	s_nop 1
	v_add_f32_dpp v227, v231, v227 quad_perm:[2,3,0,1] row_mask:0xf bank_mask:0xf bound_ctrl:1
	v_cvt_f16_f32_e32 v227, v227
	ds_write_b16 v14, v227 offset:6528
	s_waitcnt vmcnt(0)
	v_add_f32_e32 v240, v240, v241
	v_add_f32_e32 v242, v242, v243
	v_add_f32_e32 v244, v244, v245
	v_add_f32_e32 v246, v246, v247
	v_add_f32_e32 v248, v248, v249
	v_add_f32_e32 v250, v250, v251
	v_add_f32_e32 v252, v252, v253
	v_add_f32_e32 v254, v254, v255
	v_add_f32_e32 v240, v240, v242
	v_add_f32_e32 v244, v244, v246
	v_add_f32_e32 v248, v248, v250
	v_add_f32_e32 v252, v252, v254
	v_cndmask_b32_e64 v242, v240, v244, s[30:31]
	v_cndmask_b32_e64 v246, v248, v252, s[30:31]
	v_cndmask_b32_e64 v241, v244, v240, s[30:31]
	v_cndmask_b32_e64 v245, v252, v248, s[30:31]
	v_add_f32_dpp v241, v242, v241 quad_perm:[1,0,3,2] row_mask:0xf bank_mask:0xf bound_ctrl:1
	v_add_f32_dpp v245, v246, v245 quad_perm:[1,0,3,2] row_mask:0xf bank_mask:0xf bound_ctrl:1
	v_cndmask_b32_e64 v247, v241, v245, s[32:33]
	v_cndmask_b32_e64 v243, v245, v241, s[32:33]
	s_nop 1
	v_add_f32_dpp v243, v247, v243 quad_perm:[2,3,0,1] row_mask:0xf bank_mask:0xf bound_ctrl:1
	v_cvt_f16_f32_e32 v243, v243
	ds_write_b16 v14, v243 offset:7616
	s_waitcnt lgkmcnt(0)
	s_barrier
	ds_read_b128 v[160:163], v15 offset:0
	ds_read_b128 v[164:167], v15 offset:32
	ds_read_b128 v[168:171], v15 offset:64
	ds_read_b128 v[172:175], v15 offset:96
	ds_read_b128 v[176:179], v15 offset:128
	ds_read_b128 v[180:183], v15 offset:160
	ds_read_b128 v[184:187], v15 offset:192
	ds_read_b128 v[188:191], v15 offset:224
	s_waitcnt lgkmcnt(7)
	v_mfma_f32_32x32x16_f16 v[128:143], v[160:163], v[32:35], 0
	v_mfma_f32_32x32x16_f16 v[144:159], v[160:163], v[64:67], 0
	s_waitcnt lgkmcnt(6)
	v_mfma_f32_32x32x16_f16 v[128:143], v[164:167], v[36:39], v[128:143]
	v_mfma_f32_32x32x16_f16 v[144:159], v[164:167], v[68:71], v[144:159]
	s_waitcnt lgkmcnt(5)
	v_mfma_f32_32x32x16_f16 v[128:143], v[168:171], v[40:43], v[128:143]
	v_mfma_f32_32x32x16_f16 v[144:159], v[168:171], v[72:75], v[144:159]
	s_waitcnt lgkmcnt(4)
	v_mfma_f32_32x32x16_f16 v[128:143], v[172:175], v[44:47], v[128:143]
	v_mfma_f32_32x32x16_f16 v[144:159], v[172:175], v[76:79], v[144:159]
	s_waitcnt lgkmcnt(3)
	v_mfma_f32_32x32x16_f16 v[128:143], v[176:179], v[48:51], v[128:143]
	v_mfma_f32_32x32x16_f16 v[144:159], v[176:179], v[80:83], v[144:159]
	s_waitcnt lgkmcnt(2)
	v_mfma_f32_32x32x16_f16 v[128:143], v[180:183], v[52:55], v[128:143]
	v_mfma_f32_32x32x16_f16 v[144:159], v[180:183], v[84:87], v[144:159]
	s_waitcnt lgkmcnt(1)
	v_mfma_f32_32x32x16_f16 v[128:143], v[184:187], v[56:59], v[128:143]
	v_mfma_f32_32x32x16_f16 v[144:159], v[184:187], v[88:91], v[144:159]
	s_waitcnt lgkmcnt(0)
	v_mfma_f32_32x32x16_f16 v[128:143], v[188:191], v[60:63], v[128:143]
	v_mfma_f32_32x32x16_f16 v[144:159], v[188:191], v[92:95], v[144:159]
	s_nop 15
	s_nop 3
	v_mul_f32_e32 v16, v96, v128
	v_mul_f32_e32 v17, v97, v129
	v_mul_f32_e32 v18, v98, v130
	v_mul_f32_e32 v19, v99, v131
	v_fma_f32 v16, -v112, v144, v16
	v_fma_f32 v17, -v113, v145, v17
	v_fma_f32 v18, -v114, v146, v18
	v_fma_f32 v19, -v115, v147, v19
	v_fma_f32 v16, v100, v132, v16
	v_fma_f32 v16, -v116, v148, v16
	v_fma_f32 v17, v101, v133, v17
	v_fma_f32 v17, -v117, v149, v17
	v_fma_f32 v18, v102, v134, v18
	v_fma_f32 v18, -v118, v150, v18
	v_fma_f32 v19, v103, v135, v19
	v_fma_f32 v19, -v119, v151, v19
	v_fma_f32 v16, v104, v136, v16
	v_fma_f32 v16, -v120, v152, v16
	v_fma_f32 v17, v105, v137, v17
	v_fma_f32 v17, -v121, v153, v17
	v_fma_f32 v18, v106, v138, v18
	v_fma_f32 v18, -v122, v154, v18
	v_fma_f32 v19, v107, v139, v19
	v_fma_f32 v19, -v123, v155, v19
	v_fma_f32 v16, v108, v140, v16
	v_fma_f32 v16, -v124, v156, v16
	v_fma_f32 v17, v109, v141, v17
	v_fma_f32 v17, -v125, v157, v17
	v_fma_f32 v18, v110, v142, v18
	v_fma_f32 v18, -v126, v158, v18
	v_fma_f32 v19, v111, v143, v19
	v_fma_f32 v19, -v127, v159, v19
	v_add_f32_e32 v16, v16, v17
	v_add_f32_e32 v18, v18, v19
	v_add_f32_e32 v16, v16, v18
	v_mov_b32_e32 v17, v16
	s_lshl_b32 s6, s6, 6
	s_add_i32 s6, s6, s7
	s_lshl_b32 s6, s6, 10
	v_permlane32_swap_b32_e32 v16, v17
	v_add_u32_e32 v5, s6, v5
	v_cmp_gt_u32_e32 vcc, 32, v1
	v_add_f32_e32 v16, v16, v17
	s_and_saveexec_b64 s[2:3], vcc
	s_cbranch_execz .Ldog_main_done
	global_store_dword v5, v16, s[26:27]

	.amdhsa_kernel _Z8dog_mainPKfS0_S0_S0_S0_S0_S0_Pf
		.amdhsa_group_segment_fixed_size 8704
		.amdhsa_private_segment_fixed_size 0
		.amdhsa_kernarg_size 64
		.amdhsa_user_sgpr_count 2
		.amdhsa_user_sgpr_dispatch_ptr 0
		.amdhsa_user_sgpr_queue_ptr 0
		.amdhsa_user_sgpr_kernarg_segment_ptr 1
		.amdhsa_user_sgpr_dispatch_id 0
		.amdhsa_user_sgpr_kernarg_preload_length 0
		.amdhsa_user_sgpr_kernarg_preload_offset 0
		.amdhsa_user_sgpr_private_segment_size 0
		.amdhsa_uses_dynamic_stack 0
		.amdhsa_enable_private_segment 0
		.amdhsa_system_sgpr_workgroup_id_x 1
		.amdhsa_system_sgpr_workgroup_id_y 0
		.amdhsa_system_sgpr_workgroup_id_z 0
		.amdhsa_system_sgpr_workgroup_info 0
		.amdhsa_system_vgpr_workitem_id 0
		.amdhsa_next_free_vgpr 256
		.amdhsa_next_free_sgpr 96
		.amdhsa_accum_offset 256
		.amdhsa_reserve_vcc 1
		.amdhsa_float_round_mode_32 0
		.amdhsa_float_round_mode_16_64 0
		.amdhsa_float_denorm_mode_32 3
		.amdhsa_float_denorm_mode_16_64 3
		.amdhsa_dx10_clamp 1
		.amdhsa_ieee_mode 1
		.amdhsa_fp16_overflow 0
		.amdhsa_tg_split 0
		.amdhsa_exception_fp_ieee_invalid_op 0
		.amdhsa_exception_fp_denorm_src 0
		.amdhsa_exception_fp_ieee_div_zero 0
		.amdhsa_exception_fp_ieee_overflow 0
		.amdhsa_exception_fp_ieee_underflow 0
		.amdhsa_exception_fp_ieee_inexact 0
		.amdhsa_exception_int_div_zero 0
	.end_amdhsa_kernel

.Lfunc_end0:
	.size	_Z8dog_mainPKfS0_S0_S0_S0_S0_S0_Pf, .Lfunc_end0-_Z8dog_mainPKfS0_S0_S0_S0_S0_S0_Pf
	.set _Z8dog_mainPKfS0_S0_S0_S0_S0_S0_Pf.num_vgpr, 256
	.set _Z8dog_mainPKfS0_S0_S0_S0_S0_S0_Pf.num_agpr, 0
	.set _Z8dog_mainPKfS0_S0_S0_S0_S0_S0_Pf.numbered_sgpr, 44
	.set _Z8dog_mainPKfS0_S0_S0_S0_S0_S0_Pf.num_named_barrier, 0
	.set _Z8dog_mainPKfS0_S0_S0_S0_S0_S0_Pf.private_seg_size, 0
	.set _Z8dog_mainPKfS0_S0_S0_S0_S0_S0_Pf.uses_vcc, 1
	.set _Z8dog_mainPKfS0_S0_S0_S0_S0_S0_Pf.uses_flat_scratch, 0
	.set _Z8dog_mainPKfS0_S0_S0_S0_S0_S0_Pf.has_dyn_sized_stack, 0
	.set _Z8dog_mainPKfS0_S0_S0_S0_S0_S0_Pf.has_recursion, 0
	.set _Z8dog_mainPKfS0_S0_S0_S0_S0_S0_Pf.has_indirect_call, 0

amdhsa.kernels:
  - .agpr_count:     0
    .args:
      - .address_space:  global
        .offset:         0
        .size:           8
        .value_kind:     global_buffer
      - .address_space:  global
        .offset:         8
        .size:           8
        .value_kind:     global_buffer
      - .address_space:  global
        .offset:         16
        .size:           8
        .value_kind:     global_buffer
      - .address_space:  global
        .offset:         24
        .size:           8
        .value_kind:     global_buffer
      - .address_space:  global
        .offset:         32
        .size:           8
        .value_kind:     global_buffer
      - .address_space:  global
        .offset:         40
        .size:           8
        .value_kind:     global_buffer
      - .address_space:  global
        .offset:         48
        .size:           8
        .value_kind:     global_buffer
      - .actual_access:  write_only
        .address_space:  global
        .offset:         56
        .size:           8
        .value_kind:     global_buffer
    .group_segment_fixed_size: 8704
    .kernarg_segment_align: 8
    .kernarg_segment_size: 64
    .language:       OpenCL C
    .language_version:
      - 2
      - 0
    .max_flat_workgroup_size: 512
    .name:           _Z8dog_mainPKfS0_S0_S0_S0_S0_S0_Pf
    .private_segment_fixed_size: 0
    .sgpr_count:     50
    .sgpr_spill_count: 0
    .symbol:         _Z8dog_mainPKfS0_S0_S0_S0_S0_S0_Pf.kd
    .uniform_work_group_size: 1
    .uses_dynamic_stack: false
    .vgpr_count:     256
    .vgpr_spill_count: 0
    .wavefront_size: 64
  - .agpr_count:     0
    .args:
      - .actual_access:  read_only
        .address_space:  global
        .offset:         0
        .size:           8
        .value_kind:     global_buffer
      - .actual_access:  read_only
        .address_space:  global
        .offset:         8
        .size:           8
        .value_kind:     global_buffer
      - .actual_access:  write_only
        .address_space:  global
        .offset:         16
        .size:           8
        .value_kind:     global_buffer
    .group_segment_fixed_size: 0
    .kernarg_segment_align: 8
    .kernarg_segment_size: 24
    .language:       OpenCL C
    .language_version:
      - 2
      - 0
    .max_flat_workgroup_size: 256
    .name:           _Z7dog_finPKfS0_Pf
    .private_segment_fixed_size: 0
    .sgpr_count:     16
    .sgpr_spill_count: 0
    .symbol:         _Z7dog_finPKfS0_Pf.kd
    .uniform_work_group_size: 1
    .uses_dynamic_stack: false
    .vgpr_count:     16
    .vgpr_spill_count: 0
    .wavefront_size: 64
